# attention unit epilogues (global, NA, window): normalised bf16 output staged through a wave-private LDS slot and written as 8 row-contiguous 16-byte stores per lane instead of 64 two-byte stores
# speedup vs baseline: 1.0021x; 1.0021x over previous
.LBB0_582:
	s_or_b64 exec, exec, s[2:3]
	s_waitcnt lgkmcnt(0)
	v_add_u32_e32 v72, v144, v184
	ds_read_b128 v[64:67], v72
	ds_read_b128 v[68:71], v72 offset:32
	s_add_u32 s0, s20, s0
	v_ashrrev_i32_e32 v183, 31, v182
	s_addc_u32 s1, s21, s1
	s_waitcnt lgkmcnt(1)
	v_rcp_f32_e32 v73, v64
	v_rcp_f32_e32 v74, v65
	v_rcp_f32_e32 v75, v66
	v_rcp_f32_e32 v76, v67
	ds_read_b128 v[64:67], v72 offset:64
	s_waitcnt lgkmcnt(1)
	v_rcp_f32_e32 v77, v68
	v_rcp_f32_e32 v78, v69
	v_rcp_f32_e32 v79, v70
	v_rcp_f32_e32 v80, v71
	ds_read_b128 v[68:71], v72 offset:96
	s_waitcnt lgkmcnt(1)
	v_rcp_f32_e32 v72, v64
	v_rcp_f32_e32 v81, v65
	v_lshlrev_b64 v[64:65], 12, v[182:183]
	v_lshl_add_u64 v[64:65], s[0:1], 0, v[64:65]
	v_lshlrev_b32_e32 v192, 1, v200
	v_rcp_f32_e32 v82, v66
	v_rcp_f32_e32 v83, v67
	v_lshlrev_b32_e32 v66, 14, v201
	v_lshl_add_u64 v[64:65], v[64:65], 0, v[192:193]
	v_mov_b32_e32 v67, v193
	v_lshl_add_u64 v[64:65], v[64:65], 0, v[66:67]
	v_add_u32_e32 v116, v144, v184
	ds_read_b128 v[100:103], v116
	ds_read_b128 v[104:107], v116 offset:32
	ds_read_b128 v[108:111], v116 offset:64
	ds_read_b128 v[112:115], v116 offset:96
	v_readlane_b32 s100, v254, 6
	s_lshl_b32 s100, s100, 7
	s_add_i32 s100, s100, 0x12000
	v_lshlrev_b32_e32 v117, 10, v201
	v_lshl_add_u32 v117, v200, 1, v117
	v_add_u32_e32 v117, s100, v117
	v_lshlrev_b32_e32 v118, 9, v201
	v_lshl_add_u32 v118, v200, 4, v118
	v_add_u32_e32 v118, s100, v118
	v_lshlrev_b64 v[120:121], 12, v[182:183]
	v_lshl_add_u64 v[120:121], s[0:1], 0, v[120:121]
	v_lshrrev_b32_e32 v122, 4, v200
	v_lshl_add_u32 v122, v201, 1, v122
	v_lshlrev_b32_e32 v122, 12, v122
	v_and_b32_e32 v124, 15, v200
	v_lshl_add_u32 v122, v124, 4, v122
	v_mov_b32_e32 v123, 0
	v_lshl_add_u64 v[120:121], v[120:121], 0, v[122:123]
	v_mov_b32_e32 v124, 0x4000
	v_mov_b32_e32 v125, 0
	s_waitcnt lgkmcnt(0)
	v_rcp_f32_e32 v100, v100
	v_rcp_f32_e32 v101, v101
	v_rcp_f32_e32 v102, v102
	v_rcp_f32_e32 v103, v103
	v_rcp_f32_e32 v104, v104
	v_rcp_f32_e32 v105, v105
	v_rcp_f32_e32 v106, v106
	v_rcp_f32_e32 v107, v107
	v_rcp_f32_e32 v108, v108
	v_rcp_f32_e32 v109, v109
	v_rcp_f32_e32 v110, v110
	v_rcp_f32_e32 v111, v111
	v_rcp_f32_e32 v112, v112
	v_rcp_f32_e32 v113, v113
	v_rcp_f32_e32 v114, v114
	v_rcp_f32_e32 v115, v115
	v_mul_f32_e32 v126, v0, v100
	v_cvt_pk_bf16_f32 v126, v126, v126
	ds_write_b16 v117, v126 offset:0
	v_mul_f32_e32 v126, v16, v100
	v_cvt_pk_bf16_f32 v126, v126, v126
	ds_write_b16 v117, v126 offset:64
	v_mul_f32_e32 v126, v32, v100
	v_cvt_pk_bf16_f32 v126, v126, v126
	ds_write_b16 v117, v126 offset:128
	v_mul_f32_e32 v126, v48, v100
	v_cvt_pk_bf16_f32 v126, v126, v126
	ds_write_b16 v117, v126 offset:192
	v_mul_f32_e32 v126, v1, v101
	v_cvt_pk_bf16_f32 v126, v126, v126
	ds_write_b16 v117, v126 offset:256
	v_mul_f32_e32 v126, v17, v101
	v_cvt_pk_bf16_f32 v126, v126, v126
	ds_write_b16 v117, v126 offset:320
	v_mul_f32_e32 v126, v33, v101
	v_cvt_pk_bf16_f32 v126, v126, v126
	ds_write_b16 v117, v126 offset:384
	v_mul_f32_e32 v126, v49, v101
	v_cvt_pk_bf16_f32 v126, v126, v126
	ds_write_b16 v117, v126 offset:448
	v_mul_f32_e32 v126, v2, v102
	v_cvt_pk_bf16_f32 v126, v126, v126
	ds_write_b16 v117, v126 offset:512
	v_mul_f32_e32 v126, v18, v102
	v_cvt_pk_bf16_f32 v126, v126, v126
	ds_write_b16 v117, v126 offset:576
	v_mul_f32_e32 v126, v34, v102
	v_cvt_pk_bf16_f32 v126, v126, v126
	ds_write_b16 v117, v126 offset:640
	v_mul_f32_e32 v126, v50, v102
	v_cvt_pk_bf16_f32 v126, v126, v126
	ds_write_b16 v117, v126 offset:704
	v_mul_f32_e32 v126, v3, v103
	v_cvt_pk_bf16_f32 v126, v126, v126
	ds_write_b16 v117, v126 offset:768
	v_mul_f32_e32 v126, v19, v103
	v_cvt_pk_bf16_f32 v126, v126, v126
	ds_write_b16 v117, v126 offset:832
	v_mul_f32_e32 v126, v35, v103
	v_cvt_pk_bf16_f32 v126, v126, v126
	ds_write_b16 v117, v126 offset:896
	v_mul_f32_e32 v126, v51, v103
	v_cvt_pk_bf16_f32 v126, v126, v126
	ds_write_b16 v117, v126 offset:960
	v_mul_f32_e32 v126, v4, v104
	v_cvt_pk_bf16_f32 v126, v126, v126
	ds_write_b16 v117, v126 offset:2048
	v_mul_f32_e32 v126, v20, v104
	v_cvt_pk_bf16_f32 v126, v126, v126
	ds_write_b16 v117, v126 offset:2112
	v_mul_f32_e32 v126, v36, v104
	v_cvt_pk_bf16_f32 v126, v126, v126
	ds_write_b16 v117, v126 offset:2176
	v_mul_f32_e32 v126, v52, v104
	v_cvt_pk_bf16_f32 v126, v126, v126
	ds_write_b16 v117, v126 offset:2240
	v_mul_f32_e32 v126, v5, v105
	v_cvt_pk_bf16_f32 v126, v126, v126
	ds_write_b16 v117, v126 offset:2304
	v_mul_f32_e32 v126, v21, v105
	v_cvt_pk_bf16_f32 v126, v126, v126
	ds_write_b16 v117, v126 offset:2368
	v_mul_f32_e32 v126, v37, v105
	v_cvt_pk_bf16_f32 v126, v126, v126
	ds_write_b16 v117, v126 offset:2432
	v_mul_f32_e32 v126, v53, v105
	v_cvt_pk_bf16_f32 v126, v126, v126
	ds_write_b16 v117, v126 offset:2496
	v_mul_f32_e32 v126, v6, v106
	v_cvt_pk_bf16_f32 v126, v126, v126
	ds_write_b16 v117, v126 offset:2560
	v_mul_f32_e32 v126, v22, v106
	v_cvt_pk_bf16_f32 v126, v126, v126
	ds_write_b16 v117, v126 offset:2624
	v_mul_f32_e32 v126, v38, v106
	v_cvt_pk_bf16_f32 v126, v126, v126
	ds_write_b16 v117, v126 offset:2688
	v_mul_f32_e32 v126, v54, v106
	v_cvt_pk_bf16_f32 v126, v126, v126
	ds_write_b16 v117, v126 offset:2752
	v_mul_f32_e32 v126, v7, v107
	v_cvt_pk_bf16_f32 v126, v126, v126
	ds_write_b16 v117, v126 offset:2816
	v_mul_f32_e32 v126, v23, v107
	v_cvt_pk_bf16_f32 v126, v126, v126
	ds_write_b16 v117, v126 offset:2880
	v_mul_f32_e32 v126, v39, v107
	v_cvt_pk_bf16_f32 v126, v126, v126
	ds_write_b16 v117, v126 offset:2944
	v_mul_f32_e32 v126, v55, v107
	v_cvt_pk_bf16_f32 v126, v126, v126
	ds_write_b16 v117, v126 offset:3008
	v_mul_f32_e32 v126, v8, v108
	v_cvt_pk_bf16_f32 v126, v126, v126
	ds_write_b16 v117, v126 offset:4096
	v_mul_f32_e32 v126, v24, v108
	v_cvt_pk_bf16_f32 v126, v126, v126
	ds_write_b16 v117, v126 offset:4160
	v_mul_f32_e32 v126, v40, v108
	v_cvt_pk_bf16_f32 v126, v126, v126
	ds_write_b16 v117, v126 offset:4224
	v_mul_f32_e32 v126, v56, v108
	v_cvt_pk_bf16_f32 v126, v126, v126
	ds_write_b16 v117, v126 offset:4288
	v_mul_f32_e32 v126, v9, v109
	v_cvt_pk_bf16_f32 v126, v126, v126
	ds_write_b16 v117, v126 offset:4352
	v_mul_f32_e32 v126, v25, v109
	v_cvt_pk_bf16_f32 v126, v126, v126
	ds_write_b16 v117, v126 offset:4416
	v_mul_f32_e32 v126, v41, v109
	v_cvt_pk_bf16_f32 v126, v126, v126
	ds_write_b16 v117, v126 offset:4480
	v_mul_f32_e32 v126, v57, v109
	v_cvt_pk_bf16_f32 v126, v126, v126
	ds_write_b16 v117, v126 offset:4544
	v_mul_f32_e32 v126, v10, v110
	v_cvt_pk_bf16_f32 v126, v126, v126
	ds_write_b16 v117, v126 offset:4608
	v_mul_f32_e32 v126, v26, v110
	v_cvt_pk_bf16_f32 v126, v126, v126
	ds_write_b16 v117, v126 offset:4672
	v_mul_f32_e32 v126, v42, v110
	v_cvt_pk_bf16_f32 v126, v126, v126
	ds_write_b16 v117, v126 offset:4736
	v_mul_f32_e32 v126, v58, v110
	v_cvt_pk_bf16_f32 v126, v126, v126
	ds_write_b16 v117, v126 offset:4800
	v_mul_f32_e32 v126, v11, v111
	v_cvt_pk_bf16_f32 v126, v126, v126
	ds_write_b16 v117, v126 offset:4864
	v_mul_f32_e32 v126, v27, v111
	v_cvt_pk_bf16_f32 v126, v126, v126
	ds_write_b16 v117, v126 offset:4928
	v_mul_f32_e32 v126, v43, v111
	v_cvt_pk_bf16_f32 v126, v126, v126
	ds_write_b16 v117, v126 offset:4992
	v_mul_f32_e32 v126, v59, v111
	v_cvt_pk_bf16_f32 v126, v126, v126
	ds_write_b16 v117, v126 offset:5056
	v_mul_f32_e32 v126, v12, v112
	v_cvt_pk_bf16_f32 v126, v126, v126
	ds_write_b16 v117, v126 offset:6144
	v_mul_f32_e32 v126, v28, v112
	v_cvt_pk_bf16_f32 v126, v126, v126
	ds_write_b16 v117, v126 offset:6208
	v_mul_f32_e32 v126, v44, v112
	v_cvt_pk_bf16_f32 v126, v126, v126
	ds_write_b16 v117, v126 offset:6272
	v_mul_f32_e32 v126, v60, v112
	v_cvt_pk_bf16_f32 v126, v126, v126
	ds_write_b16 v117, v126 offset:6336
	v_mul_f32_e32 v126, v13, v113
	v_cvt_pk_bf16_f32 v126, v126, v126
	ds_write_b16 v117, v126 offset:6400
	v_mul_f32_e32 v126, v29, v113
	v_cvt_pk_bf16_f32 v126, v126, v126
	ds_write_b16 v117, v126 offset:6464
	v_mul_f32_e32 v126, v45, v113
	v_cvt_pk_bf16_f32 v126, v126, v126
	ds_write_b16 v117, v126 offset:6528
	v_mul_f32_e32 v126, v61, v113
	v_cvt_pk_bf16_f32 v126, v126, v126
	ds_write_b16 v117, v126 offset:6592
	v_mul_f32_e32 v126, v14, v114
	v_cvt_pk_bf16_f32 v126, v126, v126
	ds_write_b16 v117, v126 offset:6656
	v_mul_f32_e32 v126, v30, v114
	v_cvt_pk_bf16_f32 v126, v126, v126
	ds_write_b16 v117, v126 offset:6720
	v_mul_f32_e32 v126, v46, v114
	v_cvt_pk_bf16_f32 v126, v126, v126
	ds_write_b16 v117, v126 offset:6784
	v_mul_f32_e32 v126, v62, v114
	v_cvt_pk_bf16_f32 v126, v126, v126
	ds_write_b16 v117, v126 offset:6848
	v_mul_f32_e32 v126, v15, v115
	v_cvt_pk_bf16_f32 v126, v126, v126
	ds_write_b16 v117, v126 offset:6912
	v_mul_f32_e32 v126, v31, v115
	v_cvt_pk_bf16_f32 v126, v126, v126
	ds_write_b16 v117, v126 offset:6976
	v_mul_f32_e32 v126, v47, v115
	v_cvt_pk_bf16_f32 v126, v126, v126
	ds_write_b16 v117, v126 offset:7040
	v_mul_f32_e32 v126, v63, v115
	v_cvt_pk_bf16_f32 v126, v126, v126
	ds_write_b16 v117, v126 offset:7104
	s_waitcnt lgkmcnt(0)
	ds_read_b128 v[84:87], v118
	ds_read_b128 v[88:91], v118 offset:1024
	ds_read_b128 v[92:95], v118 offset:2048
	ds_read_b128 v[96:99], v118 offset:3072
	ds_read_b128 v[128:131], v118 offset:4096
	ds_read_b128 v[132:135], v118 offset:5120
	ds_read_b128 v[136:139], v118 offset:6144
	ds_read_b128 v[140:143], v118 offset:7168
	s_waitcnt lgkmcnt(7)
	global_store_dwordx4 v[120:121], v[84:87], off offset:1536
	v_lshl_add_u64 v[120:121], v[120:121], 0, v[124:125]
	s_waitcnt lgkmcnt(6)
	global_store_dwordx4 v[120:121], v[88:91], off offset:1536
	v_lshl_add_u64 v[120:121], v[120:121], 0, v[124:125]
	s_waitcnt lgkmcnt(5)
	global_store_dwordx4 v[120:121], v[92:95], off offset:1536
	v_lshl_add_u64 v[120:121], v[120:121], 0, v[124:125]
	s_waitcnt lgkmcnt(4)
	global_store_dwordx4 v[120:121], v[96:99], off offset:1536
	v_lshl_add_u64 v[120:121], v[120:121], 0, v[124:125]
	s_waitcnt lgkmcnt(3)
	global_store_dwordx4 v[120:121], v[128:131], off offset:1536
	v_lshl_add_u64 v[120:121], v[120:121], 0, v[124:125]
	s_waitcnt lgkmcnt(2)
	global_store_dwordx4 v[120:121], v[132:135], off offset:1536
	v_lshl_add_u64 v[120:121], v[120:121], 0, v[124:125]
	s_waitcnt lgkmcnt(1)
	global_store_dwordx4 v[120:121], v[136:139], off offset:1536
	v_lshl_add_u64 v[120:121], v[120:121], 0, v[124:125]
	s_waitcnt lgkmcnt(0)
	global_store_dwordx4 v[120:121], v[140:143], off offset:1536
	s_waitcnt vmcnt(63) expcnt(7) lgkmcnt(15)
	s_barrier

.LBB0_600:
	s_or_b64 exec, exec, s[0:1]
	s_waitcnt lgkmcnt(0)
	v_add_u32_e32 v72, v159, v148
	ds_read_b128 v[64:67], v72
	ds_read_b128 v[68:71], v72 offset:32
	v_readlane_b32 s0, v255, 10
	v_readlane_b32 s1, v255, 11
	s_lshl_b64 s[0:1], s[0:1], 12
	s_waitcnt lgkmcnt(1)
	v_rcp_f32_e32 v73, v64
	v_rcp_f32_e32 v74, v65
	v_rcp_f32_e32 v75, v66
	v_rcp_f32_e32 v76, v67
	ds_read_b128 v[64:67], v72 offset:64
	v_readlane_b32 s2, v254, 42
	s_add_u32 s0, s2, s0
	v_readlane_b32 s2, v254, 44
	s_addc_u32 s1, s2, s1
	v_readlane_b32 s2, v255, 12
	v_readlane_b32 s3, v255, 13
	s_add_u32 s0, s0, s2
	v_ashrrev_i32_e32 v153, 31, v152
	s_addc_u32 s1, s1, s3
	s_waitcnt lgkmcnt(1)
	v_rcp_f32_e32 v77, v68
	v_rcp_f32_e32 v78, v69
	v_rcp_f32_e32 v79, v70
	v_rcp_f32_e32 v80, v71
	ds_read_b128 v[68:71], v72 offset:96
	s_waitcnt lgkmcnt(1)
	v_rcp_f32_e32 v72, v64
	v_rcp_f32_e32 v81, v65
	v_lshlrev_b64 v[64:65], 12, v[152:153]
	v_lshl_add_u64 v[64:65], s[0:1], 0, v[64:65]
	v_lshlrev_b32_e32 v192, 1, v149
	v_rcp_f32_e32 v82, v66
	v_rcp_f32_e32 v83, v67
	v_lshlrev_b32_e32 v66, 14, v154
	v_lshl_add_u64 v[64:65], v[64:65], 0, v[192:193]
	v_mov_b32_e32 v67, v193
	v_lshl_add_u64 v[64:65], v[64:65], 0, v[66:67]
	v_add_u32_e32 v116, v159, v148
	ds_read_b128 v[100:103], v116
	ds_read_b128 v[104:107], v116 offset:32
	ds_read_b128 v[108:111], v116 offset:64
	ds_read_b128 v[112:115], v116 offset:96
	v_readlane_b32 s100, v254, 6
	s_lshl_b32 s100, s100, 7
	s_add_i32 s100, s100, 0x12000
	v_lshlrev_b32_e32 v117, 10, v154
	v_lshl_add_u32 v117, v149, 1, v117
	v_add_u32_e32 v117, s100, v117
	v_lshlrev_b32_e32 v118, 9, v154
	v_lshl_add_u32 v118, v149, 4, v118
	v_add_u32_e32 v118, s100, v118
	v_lshlrev_b64 v[120:121], 12, v[152:153]
	v_lshl_add_u64 v[120:121], s[0:1], 0, v[120:121]
	v_lshrrev_b32_e32 v122, 4, v149
	v_lshl_add_u32 v122, v154, 1, v122
	v_lshlrev_b32_e32 v122, 12, v122
	v_and_b32_e32 v124, 15, v149
	v_lshl_add_u32 v122, v124, 4, v122
	v_mov_b32_e32 v123, 0
	v_lshl_add_u64 v[120:121], v[120:121], 0, v[122:123]
	v_mov_b32_e32 v124, 0x4000
	v_mov_b32_e32 v125, 0
	s_waitcnt lgkmcnt(0)
	v_rcp_f32_e32 v100, v100
	v_rcp_f32_e32 v101, v101
	v_rcp_f32_e32 v102, v102
	v_rcp_f32_e32 v103, v103
	v_rcp_f32_e32 v104, v104
	v_rcp_f32_e32 v105, v105
	v_rcp_f32_e32 v106, v106
	v_rcp_f32_e32 v107, v107
	v_rcp_f32_e32 v108, v108
	v_rcp_f32_e32 v109, v109
	v_rcp_f32_e32 v110, v110
	v_rcp_f32_e32 v111, v111
	v_rcp_f32_e32 v112, v112
	v_rcp_f32_e32 v113, v113
	v_rcp_f32_e32 v114, v114
	v_rcp_f32_e32 v115, v115
	v_mul_f32_e32 v126, v0, v100
	v_cvt_pk_bf16_f32 v126, v126, v126
	ds_write_b16 v117, v126 offset:0
	v_mul_f32_e32 v126, v48, v100
	v_cvt_pk_bf16_f32 v126, v126, v126
	ds_write_b16 v117, v126 offset:64
	v_mul_f32_e32 v126, v32, v100
	v_cvt_pk_bf16_f32 v126, v126, v126
	ds_write_b16 v117, v126 offset:128
	v_mul_f32_e32 v126, v16, v100
	v_cvt_pk_bf16_f32 v126, v126, v126
	ds_write_b16 v117, v126 offset:192
	v_mul_f32_e32 v126, v1, v101
	v_cvt_pk_bf16_f32 v126, v126, v126
	ds_write_b16 v117, v126 offset:256
	v_mul_f32_e32 v126, v49, v101
	v_cvt_pk_bf16_f32 v126, v126, v126
	ds_write_b16 v117, v126 offset:320
	v_mul_f32_e32 v126, v33, v101
	v_cvt_pk_bf16_f32 v126, v126, v126
	ds_write_b16 v117, v126 offset:384
	v_mul_f32_e32 v126, v17, v101
	v_cvt_pk_bf16_f32 v126, v126, v126
	ds_write_b16 v117, v126 offset:448
	v_mul_f32_e32 v126, v2, v102
	v_cvt_pk_bf16_f32 v126, v126, v126
	ds_write_b16 v117, v126 offset:512
	v_mul_f32_e32 v126, v50, v102
	v_cvt_pk_bf16_f32 v126, v126, v126
	ds_write_b16 v117, v126 offset:576
	v_mul_f32_e32 v126, v34, v102
	v_cvt_pk_bf16_f32 v126, v126, v126
	ds_write_b16 v117, v126 offset:640
	v_mul_f32_e32 v126, v18, v102
	v_cvt_pk_bf16_f32 v126, v126, v126
	ds_write_b16 v117, v126 offset:704
	v_mul_f32_e32 v126, v3, v103
	v_cvt_pk_bf16_f32 v126, v126, v126
	ds_write_b16 v117, v126 offset:768
	v_mul_f32_e32 v126, v51, v103
	v_cvt_pk_bf16_f32 v126, v126, v126
	ds_write_b16 v117, v126 offset:832
	v_mul_f32_e32 v126, v35, v103
	v_cvt_pk_bf16_f32 v126, v126, v126
	ds_write_b16 v117, v126 offset:896
	v_mul_f32_e32 v126, v19, v103
	v_cvt_pk_bf16_f32 v126, v126, v126
	ds_write_b16 v117, v126 offset:960
	v_mul_f32_e32 v126, v4, v104
	v_cvt_pk_bf16_f32 v126, v126, v126
	ds_write_b16 v117, v126 offset:2048
	v_mul_f32_e32 v126, v52, v104
	v_cvt_pk_bf16_f32 v126, v126, v126
	ds_write_b16 v117, v126 offset:2112
	v_mul_f32_e32 v126, v36, v104
	v_cvt_pk_bf16_f32 v126, v126, v126
	ds_write_b16 v117, v126 offset:2176
	v_mul_f32_e32 v126, v20, v104
	v_cvt_pk_bf16_f32 v126, v126, v126
	ds_write_b16 v117, v126 offset:2240
	v_mul_f32_e32 v126, v5, v105
	v_cvt_pk_bf16_f32 v126, v126, v126
	ds_write_b16 v117, v126 offset:2304
	v_mul_f32_e32 v126, v53, v105
	v_cvt_pk_bf16_f32 v126, v126, v126
	ds_write_b16 v117, v126 offset:2368
	v_mul_f32_e32 v126, v37, v105
	v_cvt_pk_bf16_f32 v126, v126, v126
	ds_write_b16 v117, v126 offset:2432
	v_mul_f32_e32 v126, v21, v105
	v_cvt_pk_bf16_f32 v126, v126, v126
	ds_write_b16 v117, v126 offset:2496
	v_mul_f32_e32 v126, v6, v106
	v_cvt_pk_bf16_f32 v126, v126, v126
	ds_write_b16 v117, v126 offset:2560
	v_mul_f32_e32 v126, v54, v106
	v_cvt_pk_bf16_f32 v126, v126, v126
	ds_write_b16 v117, v126 offset:2624
	v_mul_f32_e32 v126, v38, v106
	v_cvt_pk_bf16_f32 v126, v126, v126
	ds_write_b16 v117, v126 offset:2688
	v_mul_f32_e32 v126, v22, v106
	v_cvt_pk_bf16_f32 v126, v126, v126
	ds_write_b16 v117, v126 offset:2752
	v_mul_f32_e32 v126, v7, v107
	v_cvt_pk_bf16_f32 v126, v126, v126
	ds_write_b16 v117, v126 offset:2816
	v_mul_f32_e32 v126, v55, v107
	v_cvt_pk_bf16_f32 v126, v126, v126
	ds_write_b16 v117, v126 offset:2880
	v_mul_f32_e32 v126, v39, v107
	v_cvt_pk_bf16_f32 v126, v126, v126
	ds_write_b16 v117, v126 offset:2944
	v_mul_f32_e32 v126, v23, v107
	v_cvt_pk_bf16_f32 v126, v126, v126
	ds_write_b16 v117, v126 offset:3008
	v_mul_f32_e32 v126, v8, v108
	v_cvt_pk_bf16_f32 v126, v126, v126
	ds_write_b16 v117, v126 offset:4096
	v_mul_f32_e32 v126, v56, v108
	v_cvt_pk_bf16_f32 v126, v126, v126
	ds_write_b16 v117, v126 offset:4160
	v_mul_f32_e32 v126, v40, v108
	v_cvt_pk_bf16_f32 v126, v126, v126
	ds_write_b16 v117, v126 offset:4224
	v_mul_f32_e32 v126, v24, v108
	v_cvt_pk_bf16_f32 v126, v126, v126
	ds_write_b16 v117, v126 offset:4288
	v_mul_f32_e32 v126, v9, v109
	v_cvt_pk_bf16_f32 v126, v126, v126
	ds_write_b16 v117, v126 offset:4352
	v_mul_f32_e32 v126, v57, v109
	v_cvt_pk_bf16_f32 v126, v126, v126
	ds_write_b16 v117, v126 offset:4416
	v_mul_f32_e32 v126, v41, v109
	v_cvt_pk_bf16_f32 v126, v126, v126
	ds_write_b16 v117, v126 offset:4480
	v_mul_f32_e32 v126, v25, v109
	v_cvt_pk_bf16_f32 v126, v126, v126
	ds_write_b16 v117, v126 offset:4544
	v_mul_f32_e32 v126, v10, v110
	v_cvt_pk_bf16_f32 v126, v126, v126
	ds_write_b16 v117, v126 offset:4608
	v_mul_f32_e32 v126, v58, v110
	v_cvt_pk_bf16_f32 v126, v126, v126
	ds_write_b16 v117, v126 offset:4672
	v_mul_f32_e32 v126, v42, v110
	v_cvt_pk_bf16_f32 v126, v126, v126
	ds_write_b16 v117, v126 offset:4736
	v_mul_f32_e32 v126, v26, v110
	v_cvt_pk_bf16_f32 v126, v126, v126
	ds_write_b16 v117, v126 offset:4800
	v_mul_f32_e32 v126, v11, v111
	v_cvt_pk_bf16_f32 v126, v126, v126
	ds_write_b16 v117, v126 offset:4864
	v_mul_f32_e32 v126, v59, v111
	v_cvt_pk_bf16_f32 v126, v126, v126
	ds_write_b16 v117, v126 offset:4928
	v_mul_f32_e32 v126, v43, v111
	v_cvt_pk_bf16_f32 v126, v126, v126
	ds_write_b16 v117, v126 offset:4992
	v_mul_f32_e32 v126, v27, v111
	v_cvt_pk_bf16_f32 v126, v126, v126
	ds_write_b16 v117, v126 offset:5056
	v_mul_f32_e32 v126, v12, v112
	v_cvt_pk_bf16_f32 v126, v126, v126
	ds_write_b16 v117, v126 offset:6144
	v_mul_f32_e32 v126, v60, v112
	v_cvt_pk_bf16_f32 v126, v126, v126
	ds_write_b16 v117, v126 offset:6208
	v_mul_f32_e32 v126, v44, v112
	v_cvt_pk_bf16_f32 v126, v126, v126
	ds_write_b16 v117, v126 offset:6272
	v_mul_f32_e32 v126, v28, v112
	v_cvt_pk_bf16_f32 v126, v126, v126
	ds_write_b16 v117, v126 offset:6336
	v_mul_f32_e32 v126, v13, v113
	v_cvt_pk_bf16_f32 v126, v126, v126
	ds_write_b16 v117, v126 offset:6400
	v_mul_f32_e32 v126, v61, v113
	v_cvt_pk_bf16_f32 v126, v126, v126
	ds_write_b16 v117, v126 offset:6464
	v_mul_f32_e32 v126, v45, v113
	v_cvt_pk_bf16_f32 v126, v126, v126
	ds_write_b16 v117, v126 offset:6528
	v_mul_f32_e32 v126, v29, v113
	v_cvt_pk_bf16_f32 v126, v126, v126
	ds_write_b16 v117, v126 offset:6592
	v_mul_f32_e32 v126, v14, v114
	v_cvt_pk_bf16_f32 v126, v126, v126
	ds_write_b16 v117, v126 offset:6656
	v_mul_f32_e32 v126, v62, v114
	v_cvt_pk_bf16_f32 v126, v126, v126
	ds_write_b16 v117, v126 offset:6720
	v_mul_f32_e32 v126, v46, v114
	v_cvt_pk_bf16_f32 v126, v126, v126
	ds_write_b16 v117, v126 offset:6784
	v_mul_f32_e32 v126, v30, v114
	v_cvt_pk_bf16_f32 v126, v126, v126
	ds_write_b16 v117, v126 offset:6848
	v_mul_f32_e32 v126, v15, v115
	v_cvt_pk_bf16_f32 v126, v126, v126
	ds_write_b16 v117, v126 offset:6912
	v_mul_f32_e32 v126, v63, v115
	v_cvt_pk_bf16_f32 v126, v126, v126
	ds_write_b16 v117, v126 offset:6976
	v_mul_f32_e32 v126, v47, v115
	v_cvt_pk_bf16_f32 v126, v126, v126
	ds_write_b16 v117, v126 offset:7040
	v_mul_f32_e32 v126, v31, v115
	v_cvt_pk_bf16_f32 v126, v126, v126
	ds_write_b16 v117, v126 offset:7104
	s_waitcnt lgkmcnt(0)
	ds_read_b128 v[84:87], v118
	ds_read_b128 v[88:91], v118 offset:1024
	ds_read_b128 v[92:95], v118 offset:2048
	ds_read_b128 v[96:99], v118 offset:3072
	ds_read_b128 v[128:131], v118 offset:4096
	ds_read_b128 v[132:135], v118 offset:5120
	ds_read_b128 v[136:139], v118 offset:6144
	ds_read_b128 v[140:143], v118 offset:7168
	s_waitcnt lgkmcnt(7)
	global_store_dwordx4 v[120:121], v[84:87], off
	v_lshl_add_u64 v[120:121], v[120:121], 0, v[124:125]
	s_waitcnt lgkmcnt(6)
	global_store_dwordx4 v[120:121], v[88:91], off
	v_lshl_add_u64 v[120:121], v[120:121], 0, v[124:125]
	s_waitcnt lgkmcnt(5)
	global_store_dwordx4 v[120:121], v[92:95], off
	v_lshl_add_u64 v[120:121], v[120:121], 0, v[124:125]
	s_waitcnt lgkmcnt(4)
	global_store_dwordx4 v[120:121], v[96:99], off
	v_lshl_add_u64 v[120:121], v[120:121], 0, v[124:125]
	s_waitcnt lgkmcnt(3)
	global_store_dwordx4 v[120:121], v[128:131], off
	v_lshl_add_u64 v[120:121], v[120:121], 0, v[124:125]
	s_waitcnt lgkmcnt(2)
	global_store_dwordx4 v[120:121], v[132:135], off
	v_lshl_add_u64 v[120:121], v[120:121], 0, v[124:125]
	s_waitcnt lgkmcnt(1)
	global_store_dwordx4 v[120:121], v[136:139], off
	v_lshl_add_u64 v[120:121], v[120:121], 0, v[124:125]
	s_waitcnt lgkmcnt(0)
	global_store_dwordx4 v[120:121], v[140:143], off
	v_readlane_b32 s0, v254, 47
	v_readlane_b32 s1, v255, 9
	s_add_i32 s1, s1, s0
	s_cmpk_gt_i32 s1, 0x17f
	s_waitcnt vmcnt(63) expcnt(7) lgkmcnt(15)
	s_barrier
	s_cbranch_scc1 .LBB0_631

.LBB0_633:
	s_or_b64 exec, exec, s[0:1]
	s_waitcnt lgkmcnt(0)
	v_add_u32_e32 v72, v151, v150
	ds_read_b128 v[64:67], v72
	ds_read_b128 v[68:71], v72 offset:32
	s_lshl_b64 s[0:1], s[4:5], 12
	v_readlane_b32 s2, v254, 42
	s_add_u32 s0, s2, s0
	s_waitcnt lgkmcnt(1)
	v_rcp_f32_e32 v73, v64
	v_rcp_f32_e32 v74, v65
	v_rcp_f32_e32 v75, v66
	v_rcp_f32_e32 v76, v67
	ds_read_b128 v[64:67], v72 offset:64
	v_readlane_b32 s2, v254, 44
	s_addc_u32 s1, s2, s1
	s_add_u32 s0, s0, s6
	v_ashrrev_i32_e32 v149, 31, v148
	s_addc_u32 s1, s1, s7
	s_waitcnt lgkmcnt(1)
	v_rcp_f32_e32 v77, v68
	v_rcp_f32_e32 v78, v69
	v_rcp_f32_e32 v79, v70
	v_rcp_f32_e32 v80, v71
	ds_read_b128 v[68:71], v72 offset:96
	s_waitcnt lgkmcnt(1)
	v_rcp_f32_e32 v72, v64
	v_rcp_f32_e32 v81, v65
	v_lshlrev_b64 v[64:65], 12, v[148:149]
	v_lshl_add_u64 v[64:65], s[0:1], 0, v[64:65]
	v_lshlrev_b32_e32 v192, 1, v154
	v_rcp_f32_e32 v82, v66
	v_rcp_f32_e32 v83, v67
	v_lshlrev_b32_e32 v66, 14, v155
	v_lshl_add_u64 v[64:65], v[64:65], 0, v[192:193]
	v_mov_b32_e32 v67, v193
	v_lshl_add_u64 v[64:65], v[64:65], 0, v[66:67]
	v_add_u32_e32 v116, v151, v150
	ds_read_b128 v[100:103], v116
	ds_read_b128 v[104:107], v116 offset:32
	ds_read_b128 v[108:111], v116 offset:64
	ds_read_b128 v[112:115], v116 offset:96
	v_readlane_b32 s100, v254, 6
	s_lshl_b32 s100, s100, 7
	s_add_i32 s100, s100, 0x12000
	v_lshlrev_b32_e32 v117, 10, v155
	v_lshl_add_u32 v117, v154, 1, v117
	v_add_u32_e32 v117, s100, v117
	v_lshlrev_b32_e32 v118, 9, v155
	v_lshl_add_u32 v118, v154, 4, v118
	v_add_u32_e32 v118, s100, v118
	v_lshlrev_b64 v[120:121], 12, v[148:149]
	v_lshl_add_u64 v[120:121], s[0:1], 0, v[120:121]
	v_lshrrev_b32_e32 v122, 4, v154
	v_lshl_add_u32 v122, v155, 1, v122
	v_lshlrev_b32_e32 v122, 12, v122
	v_and_b32_e32 v124, 15, v154
	v_lshl_add_u32 v122, v124, 4, v122
	v_mov_b32_e32 v123, 0
	v_lshl_add_u64 v[120:121], v[120:121], 0, v[122:123]
	v_mov_b32_e32 v124, 0x4000
	v_mov_b32_e32 v125, 0
	s_waitcnt lgkmcnt(0)
	v_rcp_f32_e32 v100, v100
	v_rcp_f32_e32 v101, v101
	v_rcp_f32_e32 v102, v102
	v_rcp_f32_e32 v103, v103
	v_rcp_f32_e32 v104, v104
	v_rcp_f32_e32 v105, v105
	v_rcp_f32_e32 v106, v106
	v_rcp_f32_e32 v107, v107
	v_rcp_f32_e32 v108, v108
	v_rcp_f32_e32 v109, v109
	v_rcp_f32_e32 v110, v110
	v_rcp_f32_e32 v111, v111
	v_rcp_f32_e32 v112, v112
	v_rcp_f32_e32 v113, v113
	v_rcp_f32_e32 v114, v114
	v_rcp_f32_e32 v115, v115
	v_mul_f32_e32 v126, v48, v100
	v_cvt_pk_bf16_f32 v126, v126, v126
	ds_write_b16 v117, v126 offset:0
	v_mul_f32_e32 v126, v32, v100
	v_cvt_pk_bf16_f32 v126, v126, v126
	ds_write_b16 v117, v126 offset:64
	v_mul_f32_e32 v126, v16, v100
	v_cvt_pk_bf16_f32 v126, v126, v126
	ds_write_b16 v117, v126 offset:128
	v_mul_f32_e32 v126, v0, v100
	v_cvt_pk_bf16_f32 v126, v126, v126
	ds_write_b16 v117, v126 offset:192
	v_mul_f32_e32 v126, v49, v101
	v_cvt_pk_bf16_f32 v126, v126, v126
	ds_write_b16 v117, v126 offset:256
	v_mul_f32_e32 v126, v33, v101
	v_cvt_pk_bf16_f32 v126, v126, v126
	ds_write_b16 v117, v126 offset:320
	v_mul_f32_e32 v126, v17, v101
	v_cvt_pk_bf16_f32 v126, v126, v126
	ds_write_b16 v117, v126 offset:384
	v_mul_f32_e32 v126, v1, v101
	v_cvt_pk_bf16_f32 v126, v126, v126
	ds_write_b16 v117, v126 offset:448
	v_mul_f32_e32 v126, v50, v102
	v_cvt_pk_bf16_f32 v126, v126, v126
	ds_write_b16 v117, v126 offset:512
	v_mul_f32_e32 v126, v34, v102
	v_cvt_pk_bf16_f32 v126, v126, v126
	ds_write_b16 v117, v126 offset:576
	v_mul_f32_e32 v126, v18, v102
	v_cvt_pk_bf16_f32 v126, v126, v126
	ds_write_b16 v117, v126 offset:640
	v_mul_f32_e32 v126, v2, v102
	v_cvt_pk_bf16_f32 v126, v126, v126
	ds_write_b16 v117, v126 offset:704
	v_mul_f32_e32 v126, v51, v103
	v_cvt_pk_bf16_f32 v126, v126, v126
	ds_write_b16 v117, v126 offset:768
	v_mul_f32_e32 v126, v35, v103
	v_cvt_pk_bf16_f32 v126, v126, v126
	ds_write_b16 v117, v126 offset:832
	v_mul_f32_e32 v126, v19, v103
	v_cvt_pk_bf16_f32 v126, v126, v126
	ds_write_b16 v117, v126 offset:896
	v_mul_f32_e32 v126, v3, v103
	v_cvt_pk_bf16_f32 v126, v126, v126
	ds_write_b16 v117, v126 offset:960
	v_mul_f32_e32 v126, v52, v104
	v_cvt_pk_bf16_f32 v126, v126, v126
	ds_write_b16 v117, v126 offset:2048
	v_mul_f32_e32 v126, v36, v104
	v_cvt_pk_bf16_f32 v126, v126, v126
	ds_write_b16 v117, v126 offset:2112
	v_mul_f32_e32 v126, v20, v104
	v_cvt_pk_bf16_f32 v126, v126, v126
	ds_write_b16 v117, v126 offset:2176
	v_mul_f32_e32 v126, v4, v104
	v_cvt_pk_bf16_f32 v126, v126, v126
	ds_write_b16 v117, v126 offset:2240
	v_mul_f32_e32 v126, v53, v105
	v_cvt_pk_bf16_f32 v126, v126, v126
	ds_write_b16 v117, v126 offset:2304
	v_mul_f32_e32 v126, v37, v105
	v_cvt_pk_bf16_f32 v126, v126, v126
	ds_write_b16 v117, v126 offset:2368
	v_mul_f32_e32 v126, v21, v105
	v_cvt_pk_bf16_f32 v126, v126, v126
	ds_write_b16 v117, v126 offset:2432
	v_mul_f32_e32 v126, v5, v105
	v_cvt_pk_bf16_f32 v126, v126, v126
	ds_write_b16 v117, v126 offset:2496
	v_mul_f32_e32 v126, v54, v106
	v_cvt_pk_bf16_f32 v126, v126, v126
	ds_write_b16 v117, v126 offset:2560
	v_mul_f32_e32 v126, v38, v106
	v_cvt_pk_bf16_f32 v126, v126, v126
	ds_write_b16 v117, v126 offset:2624
	v_mul_f32_e32 v126, v22, v106
	v_cvt_pk_bf16_f32 v126, v126, v126
	ds_write_b16 v117, v126 offset:2688
	v_mul_f32_e32 v126, v6, v106
	v_cvt_pk_bf16_f32 v126, v126, v126
	ds_write_b16 v117, v126 offset:2752
	v_mul_f32_e32 v126, v55, v107
	v_cvt_pk_bf16_f32 v126, v126, v126
	ds_write_b16 v117, v126 offset:2816
	v_mul_f32_e32 v126, v39, v107
	v_cvt_pk_bf16_f32 v126, v126, v126
	ds_write_b16 v117, v126 offset:2880
	v_mul_f32_e32 v126, v23, v107
	v_cvt_pk_bf16_f32 v126, v126, v126
	ds_write_b16 v117, v126 offset:2944
	v_mul_f32_e32 v126, v7, v107
	v_cvt_pk_bf16_f32 v126, v126, v126
	ds_write_b16 v117, v126 offset:3008
	v_mul_f32_e32 v126, v56, v108
	v_cvt_pk_bf16_f32 v126, v126, v126
	ds_write_b16 v117, v126 offset:4096
	v_mul_f32_e32 v126, v40, v108
	v_cvt_pk_bf16_f32 v126, v126, v126
	ds_write_b16 v117, v126 offset:4160
	v_mul_f32_e32 v126, v24, v108
	v_cvt_pk_bf16_f32 v126, v126, v126
	ds_write_b16 v117, v126 offset:4224
	v_mul_f32_e32 v126, v8, v108
	v_cvt_pk_bf16_f32 v126, v126, v126
	ds_write_b16 v117, v126 offset:4288
	v_mul_f32_e32 v126, v57, v109
	v_cvt_pk_bf16_f32 v126, v126, v126
	ds_write_b16 v117, v126 offset:4352
	v_mul_f32_e32 v126, v41, v109
	v_cvt_pk_bf16_f32 v126, v126, v126
	ds_write_b16 v117, v126 offset:4416
	v_mul_f32_e32 v126, v25, v109
	v_cvt_pk_bf16_f32 v126, v126, v126
	ds_write_b16 v117, v126 offset:4480
	v_mul_f32_e32 v126, v9, v109
	v_cvt_pk_bf16_f32 v126, v126, v126
	ds_write_b16 v117, v126 offset:4544
	v_mul_f32_e32 v126, v58, v110
	v_cvt_pk_bf16_f32 v126, v126, v126
	ds_write_b16 v117, v126 offset:4608
	v_mul_f32_e32 v126, v42, v110
	v_cvt_pk_bf16_f32 v126, v126, v126
	ds_write_b16 v117, v126 offset:4672
	v_mul_f32_e32 v126, v26, v110
	v_cvt_pk_bf16_f32 v126, v126, v126
	ds_write_b16 v117, v126 offset:4736
	v_mul_f32_e32 v126, v10, v110
	v_cvt_pk_bf16_f32 v126, v126, v126
	ds_write_b16 v117, v126 offset:4800
	v_mul_f32_e32 v126, v59, v111
	v_cvt_pk_bf16_f32 v126, v126, v126
	ds_write_b16 v117, v126 offset:4864
	v_mul_f32_e32 v126, v43, v111
	v_cvt_pk_bf16_f32 v126, v126, v126
	ds_write_b16 v117, v126 offset:4928
	v_mul_f32_e32 v126, v27, v111
	v_cvt_pk_bf16_f32 v126, v126, v126
	ds_write_b16 v117, v126 offset:4992
	v_mul_f32_e32 v126, v11, v111
	v_cvt_pk_bf16_f32 v126, v126, v126
	ds_write_b16 v117, v126 offset:5056
	v_mul_f32_e32 v126, v60, v112
	v_cvt_pk_bf16_f32 v126, v126, v126
	ds_write_b16 v117, v126 offset:6144
	v_mul_f32_e32 v126, v44, v112
	v_cvt_pk_bf16_f32 v126, v126, v126
	ds_write_b16 v117, v126 offset:6208
	v_mul_f32_e32 v126, v28, v112
	v_cvt_pk_bf16_f32 v126, v126, v126
	ds_write_b16 v117, v126 offset:6272
	v_mul_f32_e32 v126, v12, v112
	v_cvt_pk_bf16_f32 v126, v126, v126
	ds_write_b16 v117, v126 offset:6336
	v_mul_f32_e32 v126, v61, v113
	v_cvt_pk_bf16_f32 v126, v126, v126
	ds_write_b16 v117, v126 offset:6400
	v_mul_f32_e32 v126, v45, v113
	v_cvt_pk_bf16_f32 v126, v126, v126
	ds_write_b16 v117, v126 offset:6464
	v_mul_f32_e32 v126, v29, v113
	v_cvt_pk_bf16_f32 v126, v126, v126
	ds_write_b16 v117, v126 offset:6528
	v_mul_f32_e32 v126, v13, v113
	v_cvt_pk_bf16_f32 v126, v126, v126
	ds_write_b16 v117, v126 offset:6592
	v_mul_f32_e32 v126, v62, v114
	v_cvt_pk_bf16_f32 v126, v126, v126
	ds_write_b16 v117, v126 offset:6656
	v_mul_f32_e32 v126, v46, v114
	v_cvt_pk_bf16_f32 v126, v126, v126
	ds_write_b16 v117, v126 offset:6720
	v_mul_f32_e32 v126, v30, v114
	v_cvt_pk_bf16_f32 v126, v126, v126
	ds_write_b16 v117, v126 offset:6784
	v_mul_f32_e32 v126, v14, v114
	v_cvt_pk_bf16_f32 v126, v126, v126
	ds_write_b16 v117, v126 offset:6848
	v_mul_f32_e32 v126, v63, v115
	v_cvt_pk_bf16_f32 v126, v126, v126
	ds_write_b16 v117, v126 offset:6912
	v_mul_f32_e32 v126, v47, v115
	v_cvt_pk_bf16_f32 v126, v126, v126
	ds_write_b16 v117, v126 offset:6976
	v_mul_f32_e32 v126, v31, v115
	v_cvt_pk_bf16_f32 v126, v126, v126
	ds_write_b16 v117, v126 offset:7040
	v_mul_f32_e32 v126, v15, v115
	v_cvt_pk_bf16_f32 v126, v126, v126
	ds_write_b16 v117, v126 offset:7104
	s_waitcnt lgkmcnt(0)
	ds_read_b128 v[84:87], v118
	ds_read_b128 v[88:91], v118 offset:1024
	ds_read_b128 v[92:95], v118 offset:2048
	ds_read_b128 v[96:99], v118 offset:3072
	ds_read_b128 v[128:131], v118 offset:4096
	ds_read_b128 v[132:135], v118 offset:5120
	ds_read_b128 v[136:139], v118 offset:6144
	ds_read_b128 v[140:143], v118 offset:7168
	s_waitcnt lgkmcnt(7)
	global_store_dwordx4 v[120:121], v[84:87], off offset:3072
	v_lshl_add_u64 v[120:121], v[120:121], 0, v[124:125]
	s_waitcnt lgkmcnt(6)
	global_store_dwordx4 v[120:121], v[88:91], off offset:3072
	v_lshl_add_u64 v[120:121], v[120:121], 0, v[124:125]
	s_waitcnt lgkmcnt(5)
	global_store_dwordx4 v[120:121], v[92:95], off offset:3072
	v_lshl_add_u64 v[120:121], v[120:121], 0, v[124:125]
	s_waitcnt lgkmcnt(4)
	global_store_dwordx4 v[120:121], v[96:99], off offset:3072
	v_lshl_add_u64 v[120:121], v[120:121], 0, v[124:125]
	s_waitcnt lgkmcnt(3)
	global_store_dwordx4 v[120:121], v[128:131], off offset:3072
	v_lshl_add_u64 v[120:121], v[120:121], 0, v[124:125]
	s_waitcnt lgkmcnt(2)
	global_store_dwordx4 v[120:121], v[132:135], off offset:3072
	v_lshl_add_u64 v[120:121], v[120:121], 0, v[124:125]
	s_waitcnt lgkmcnt(1)
	global_store_dwordx4 v[120:121], v[136:139], off offset:3072
	v_lshl_add_u64 v[120:121], v[120:121], 0, v[124:125]
	s_waitcnt lgkmcnt(0)
	global_store_dwordx4 v[120:121], v[140:143], off offset:3072
	v_readlane_b32 s0, v254, 47
	s_add_i32 s18, s18, s0
	s_cmpk_gt_i32 s18, 0xff
	s_waitcnt vmcnt(63) expcnt(7) lgkmcnt(15)
	s_barrier
	s_cbranch_scc1 .LBB0_665
